# speedup vs baseline: 1.0082x; 1.0027x over previous
_Z11proj_kernelPKfS0_S0_S0_S0_S0_PDF16_S1_PfS2_:
	s_load_dwordx2 s[20:21], s[0:1], 0x0
	v_lshrrev_b32_e32 v248, 7, v0
	v_bfe_u32 v249, v0, 6, 1
	v_mul_u32_u24_e32 v249, 0x60, v249
	v_lshrrev_b32_e32 v250, 2, v0
	v_and_b32_e32 v250, 8, v250
	v_or_b32_e32 v249, v249, v250
	v_lshl_add_u32 v249, v249, 7, v248
	v_and_b32_e32 v250, 31, v0
	v_lshlrev_b32_e32 v250, 4, v250
	v_lshl_add_u32 v248, v249, 9, v250
	s_bfe_u32 s22, s2, 0x20001
	s_mul_i32 s22, s22, 0x6000
	s_lshr_b32 s23, s2, 2
	s_and_b32 s23, s23, 0x3ffffffe
	s_and_b32 s24, s2, 1
	s_or_b32 s23, s23, s24
	s_lshl_b32 s23, s23, 1
	s_add_i32 s22, s22, s23
	s_lshl_b32 s22, s22, 9
	v_add_u32_e32 v248, s22, v248
	s_waitcnt lgkmcnt(0)
	global_load_dwordx4 v[184:187], v248, s[20:21]
	s_add_u32 s22, s20, 0x10000
	s_addc_u32 s23, s21, 0
	global_load_dwordx4 v[188:191], v248, s[22:23]
	s_add_u32 s22, s20, 0x20000
	s_addc_u32 s23, s21, 0
	global_load_dwordx4 v[192:195], v248, s[22:23]
	s_add_u32 s22, s20, 0x30000
	s_addc_u32 s23, s21, 0
	global_load_dwordx4 v[196:199], v248, s[22:23]
	s_add_u32 s22, s20, 0x40000
	s_addc_u32 s23, s21, 0
	global_load_dwordx4 v[200:203], v248, s[22:23]
	s_add_u32 s22, s20, 0x50000
	s_addc_u32 s23, s21, 0
	global_load_dwordx4 v[204:207], v248, s[22:23]
	s_add_u32 s22, s20, 0x60000
	s_addc_u32 s23, s21, 0
	global_load_dwordx4 v[208:211], v248, s[22:23]
	s_add_u32 s22, s20, 0x70000
	s_addc_u32 s23, s21, 0
	global_load_dwordx4 v[212:215], v248, s[22:23]
	v_and_b32_e32 v2, 15, v0
	v_bfe_u32 v1, v0, 4, 1
	v_cmp_lt_u32_e32 vcc, 11, v2
	v_mul_u32_u24_e32 v1, 14, v1
	s_and_saveexec_b64 s[4:5], vcc
	s_xor_b64 s[6:7], exec, s[4:5]
	s_cbranch_execz .LBB0_10
	v_cmp_lt_i32_e64 s[4:5], 13, v2
	s_and_saveexec_b64 s[8:9], s[4:5]
	s_xor_b64 s[8:9], exec, s[8:9]
	s_cbranch_execz .LBB0_5
	v_cmp_eq_u32_e64 s[4:5], 14, v2
	v_mov_b32_e32 v132, 0
	v_mov_b32_e32 v10, v1
	s_and_saveexec_b64 s[10:11], s[4:5]
	v_add_u32_e32 v10, 13, v1
	v_mov_b32_e32 v132, 1.0
	s_or_b64 exec, exec, s[10:11]

.LBB0_34:
	s_lshr_b32 s0, s2, 2
	s_and_b32 s0, s0, 0x3ffffffe
	s_and_b32 s1, s2, 1
	v_lshrrev_b32_e32 v143, 7, v0
	s_bfe_u32 s3, s2, 0x20001
	s_or_b32 s0, s0, s1
	v_lshl_or_b32 v133, s0, 1, v143
	s_mul_i32 s0, s3, 0xc0
	v_bfe_u32 v135, v0, 6, 1
	s_movk_i32 s1, 0x60
	v_mov_b32_e32 v2, s0
	v_lshrrev_b32_e32 v3, 2, v0
	v_mad_u32_u24 v2, v135, s1, v2
	v_and_b32_e32 v142, 8, v3
	v_or_b32_e32 v2, v2, v142
	v_lshl_add_u32 v130, v2, 7, v133
	v_mov_b32_e32 v131, 0
	v_lshlrev_b64 v[2:3], 9, v[130:131]
	v_mul_u32_u24_e32 v4, 0x60, v135
	s_waitcnt lgkmcnt(0)
	v_lshl_add_u64 v[2:3], s[4:5], 0, v[2:3]
	v_lshlrev_b32_e32 v130, 4, v1
	v_lshl_add_u64 v[136:137], v[2:3], 0, v[130:131]
	v_lshlrev_b32_e32 v130, 2, v4
	v_lshl_add_u64 v[2:3], s[6:7], 0, v[130:131]
	s_movk_i32 s2, 0x300
	v_mad_u64_u32 v[4:5], s[0:1], v11, s2, v[2:3]
	v_mad_u64_u32 v[2:3], s[0:1], v10, s2, v[2:3]
	v_lshlrev_b32_e32 v130, 2, v142
	v_lshl_add_u64 v[140:141], v[2:3], 0, v[130:131]
	v_lshl_add_u64 v[138:139], v[4:5], 0, v[130:131]
	global_load_dwordx4 v[168:171], v[140:141], off
	global_load_dwordx4 v[172:175], v[140:141], off offset:16
	global_load_dwordx4 v[176:179], v[138:139], off
	global_load_dwordx4 v[180:183], v[138:139], off offset:16
	s_mov_b32 s2, 0xffff
	s_lshl_b32 s3, s3, 16
	s_or_b32 s4, s3, 0x4000
	s_or_b32 s5, s3, 0x8000
	s_or_b32 s6, s3, 0xc000
	s_add_u32 s22, s20, 0x100000
	s_addc_u32 s23, s21, 0
	global_load_dwordx4 v[216:219], v248, s[22:23]
	s_add_u32 s22, s20, 0x110000
	s_addc_u32 s23, s21, 0
	global_load_dwordx4 v[220:223], v248, s[22:23]
	s_add_u32 s22, s20, 0x120000
	s_addc_u32 s23, s21, 0
	global_load_dwordx4 v[224:227], v248, s[22:23]
	s_add_u32 s22, s20, 0x130000
	s_addc_u32 s23, s21, 0
	global_load_dwordx4 v[228:231], v248, s[22:23]
	s_add_u32 s22, s20, 0x140000
	s_addc_u32 s23, s21, 0
	global_load_dwordx4 v[232:235], v248, s[22:23]
	s_add_u32 s22, s20, 0x150000
	s_addc_u32 s23, s21, 0
	global_load_dwordx4 v[236:239], v248, s[22:23]
	s_add_u32 s22, s20, 0x160000
	s_addc_u32 s23, s21, 0
	global_load_dwordx4 v[240:243], v248, s[22:23]
	s_add_u32 s22, s20, 0x170000
	s_addc_u32 s23, s21, 0
	global_load_dwordx4 v[244:247], v248, s[22:23]
	s_waitcnt vmcnt(8)
	v_pk_mul_f32 v[168:169], v[168:169], v[132:133] op_sel_hi:[1,0]
	v_pk_mul_f32 v[170:171], v[170:171], v[132:133] op_sel_hi:[1,0]
	v_pk_mul_f32 v[172:173], v[172:173], v[132:133] op_sel_hi:[1,0]
	v_pk_mul_f32 v[174:175], v[174:175], v[132:133] op_sel_hi:[1,0]
	v_pk_mul_f32 v[176:177], v[176:177], v[134:135] op_sel_hi:[1,0]
	v_pk_mul_f32 v[178:179], v[178:179], v[134:135] op_sel_hi:[1,0]
	v_pk_mul_f32 v[180:181], v[180:181], v[134:135] op_sel_hi:[1,0]
	v_pk_mul_f32 v[182:183], v[182:183], v[134:135] op_sel_hi:[1,0]
	v_cvt_pk_f16_f32 v144, v168, v169
	v_cvt_pk_f16_f32 v145, v170, v171
	v_cvt_pk_f16_f32 v146, v172, v173
	v_cvt_pk_f16_f32 v147, v174, v175
	v_cvt_pk_f16_f32 v148, v176, v177
	v_cvt_pk_f16_f32 v149, v178, v179
	v_cvt_pk_f16_f32 v150, v180, v181
	v_cvt_pk_f16_f32 v151, v182, v183
	global_load_dwordx4 v[168:171], v[140:141], off offset:64
	global_load_dwordx4 v[172:175], v[140:141], off offset:80
	global_load_dwordx4 v[176:179], v[138:139], off offset:64
	global_load_dwordx4 v[180:183], v[138:139], off offset:80
	v_cvt_pk_f16_f32 v152, v184, v188
	v_cvt_pk_f16_f32 v153, v192, v196
	v_cvt_pk_f16_f32 v154, v200, v204
	v_cvt_pk_f16_f32 v155, v208, v212
	v_cvt_pk_f16_f32 v156, v185, v189
	v_cvt_pk_f16_f32 v157, v193, v197
	v_cvt_pk_f16_f32 v158, v201, v205
	v_cvt_pk_f16_f32 v159, v209, v213
	v_cvt_pk_f16_f32 v160, v186, v190
	v_cvt_pk_f16_f32 v161, v194, v198
	v_cvt_pk_f16_f32 v162, v202, v206
	v_cvt_pk_f16_f32 v163, v210, v214
	v_cvt_pk_f16_f32 v164, v187, v191
	v_cvt_pk_f16_f32 v165, v195, v199
	v_cvt_pk_f16_f32 v166, v203, v207
	v_cvt_pk_f16_f32 v167, v211, v215
	s_nop 1
	v_mfma_f32_32x32x16_f16 v[98:113], v[144:147], v[152:155], 0
	v_mfma_f32_32x32x16_f16 v[66:81], v[148:151], v[152:155], 0
	v_mfma_f32_32x32x16_f16 v[34:49], v[144:147], v[156:159], 0
	v_mfma_f32_32x32x16_f16 v[2:17], v[148:151], v[156:159], 0
	v_mfma_f32_32x32x16_f16 v[114:129], v[144:147], v[160:163], 0
	v_mfma_f32_32x32x16_f16 v[82:97], v[148:151], v[160:163], 0
	v_mfma_f32_32x32x16_f16 v[50:65], v[144:147], v[164:167], 0
	v_mfma_f32_32x32x16_f16 v[18:33], v[148:151], v[164:167], 0
	s_add_u32 s22, s20, 0x200000
	s_addc_u32 s23, s21, 0
	global_load_dwordx4 v[184:187], v248, s[22:23]
	s_add_u32 s22, s20, 0x210000
	s_addc_u32 s23, s21, 0
	global_load_dwordx4 v[188:191], v248, s[22:23]
	s_add_u32 s22, s20, 0x220000
	s_addc_u32 s23, s21, 0
	global_load_dwordx4 v[192:195], v248, s[22:23]
	s_add_u32 s22, s20, 0x230000
	s_addc_u32 s23, s21, 0
	global_load_dwordx4 v[196:199], v248, s[22:23]
	s_add_u32 s22, s20, 0x240000
	s_addc_u32 s23, s21, 0
	global_load_dwordx4 v[200:203], v248, s[22:23]
	s_add_u32 s22, s20, 0x250000
	s_addc_u32 s23, s21, 0
	global_load_dwordx4 v[204:207], v248, s[22:23]
	s_add_u32 s22, s20, 0x260000
	s_addc_u32 s23, s21, 0
	global_load_dwordx4 v[208:211], v248, s[22:23]
	s_add_u32 s22, s20, 0x270000
	s_addc_u32 s23, s21, 0
	global_load_dwordx4 v[212:215], v248, s[22:23]
	s_waitcnt vmcnt(8)
	v_pk_mul_f32 v[168:169], v[168:169], v[132:133] op_sel_hi:[1,0]
	v_pk_mul_f32 v[170:171], v[170:171], v[132:133] op_sel_hi:[1,0]
	v_pk_mul_f32 v[172:173], v[172:173], v[132:133] op_sel_hi:[1,0]
	v_pk_mul_f32 v[174:175], v[174:175], v[132:133] op_sel_hi:[1,0]
	v_pk_mul_f32 v[176:177], v[176:177], v[134:135] op_sel_hi:[1,0]
	v_pk_mul_f32 v[178:179], v[178:179], v[134:135] op_sel_hi:[1,0]
	v_pk_mul_f32 v[180:181], v[180:181], v[134:135] op_sel_hi:[1,0]
	v_pk_mul_f32 v[182:183], v[182:183], v[134:135] op_sel_hi:[1,0]
	v_cvt_pk_f16_f32 v144, v168, v169
	v_cvt_pk_f16_f32 v145, v170, v171
	v_cvt_pk_f16_f32 v146, v172, v173
	v_cvt_pk_f16_f32 v147, v174, v175
	v_cvt_pk_f16_f32 v148, v176, v177
	v_cvt_pk_f16_f32 v149, v178, v179
	v_cvt_pk_f16_f32 v150, v180, v181
	v_cvt_pk_f16_f32 v151, v182, v183
	global_load_dwordx4 v[168:171], v[140:141], off offset:128
	global_load_dwordx4 v[172:175], v[140:141], off offset:144
	global_load_dwordx4 v[176:179], v[138:139], off offset:128
	global_load_dwordx4 v[180:183], v[138:139], off offset:144
	v_cvt_pk_f16_f32 v152, v216, v220
	v_cvt_pk_f16_f32 v153, v224, v228
	v_cvt_pk_f16_f32 v154, v232, v236
	v_cvt_pk_f16_f32 v155, v240, v244
	v_cvt_pk_f16_f32 v156, v217, v221
	v_cvt_pk_f16_f32 v157, v225, v229
	v_cvt_pk_f16_f32 v158, v233, v237
	v_cvt_pk_f16_f32 v159, v241, v245
	v_cvt_pk_f16_f32 v160, v218, v222
	v_cvt_pk_f16_f32 v161, v226, v230
	v_cvt_pk_f16_f32 v162, v234, v238
	v_cvt_pk_f16_f32 v163, v242, v246
	v_cvt_pk_f16_f32 v164, v219, v223
	v_cvt_pk_f16_f32 v165, v227, v231
	v_cvt_pk_f16_f32 v166, v235, v239
	v_cvt_pk_f16_f32 v167, v243, v247
	s_nop 1
	v_mfma_f32_32x32x16_f16 v[98:113], v[144:147], v[152:155], v[98:113]
	v_mfma_f32_32x32x16_f16 v[66:81], v[148:151], v[152:155], v[66:81]
	v_mfma_f32_32x32x16_f16 v[34:49], v[144:147], v[156:159], v[34:49]
	v_mfma_f32_32x32x16_f16 v[2:17], v[148:151], v[156:159], v[2:17]
	v_mfma_f32_32x32x16_f16 v[114:129], v[144:147], v[160:163], v[114:129]
	v_mfma_f32_32x32x16_f16 v[82:97], v[148:151], v[160:163], v[82:97]
	v_mfma_f32_32x32x16_f16 v[50:65], v[144:147], v[164:167], v[50:65]
	v_mfma_f32_32x32x16_f16 v[18:33], v[148:151], v[164:167], v[18:33]
	s_add_u32 s22, s20, 0x300000
	s_addc_u32 s23, s21, 0
	global_load_dwordx4 v[216:219], v248, s[22:23]
	s_add_u32 s22, s20, 0x310000
	s_addc_u32 s23, s21, 0
	global_load_dwordx4 v[220:223], v248, s[22:23]
	s_add_u32 s22, s20, 0x320000
	s_addc_u32 s23, s21, 0
	global_load_dwordx4 v[224:227], v248, s[22:23]
	s_add_u32 s22, s20, 0x330000
	s_addc_u32 s23, s21, 0
	global_load_dwordx4 v[228:231], v248, s[22:23]
	s_add_u32 s22, s20, 0x340000
	s_addc_u32 s23, s21, 0
	global_load_dwordx4 v[232:235], v248, s[22:23]
	s_add_u32 s22, s20, 0x350000
	s_addc_u32 s23, s21, 0
	global_load_dwordx4 v[236:239], v248, s[22:23]
	s_add_u32 s22, s20, 0x360000
	s_addc_u32 s23, s21, 0
	global_load_dwordx4 v[240:243], v248, s[22:23]
	s_add_u32 s22, s20, 0x370000
	s_addc_u32 s23, s21, 0
	global_load_dwordx4 v[244:247], v248, s[22:23]
	s_waitcnt vmcnt(8)
	v_pk_mul_f32 v[168:169], v[168:169], v[132:133] op_sel_hi:[1,0]
	v_pk_mul_f32 v[170:171], v[170:171], v[132:133] op_sel_hi:[1,0]
	v_pk_mul_f32 v[172:173], v[172:173], v[132:133] op_sel_hi:[1,0]
	v_pk_mul_f32 v[174:175], v[174:175], v[132:133] op_sel_hi:[1,0]
	v_pk_mul_f32 v[176:177], v[176:177], v[134:135] op_sel_hi:[1,0]
	v_pk_mul_f32 v[178:179], v[178:179], v[134:135] op_sel_hi:[1,0]
	v_pk_mul_f32 v[180:181], v[180:181], v[134:135] op_sel_hi:[1,0]
	v_pk_mul_f32 v[182:183], v[182:183], v[134:135] op_sel_hi:[1,0]
	v_cvt_pk_f16_f32 v144, v168, v169
	v_cvt_pk_f16_f32 v145, v170, v171
	v_cvt_pk_f16_f32 v146, v172, v173
	v_cvt_pk_f16_f32 v147, v174, v175
	v_cvt_pk_f16_f32 v148, v176, v177
	v_cvt_pk_f16_f32 v149, v178, v179
	v_cvt_pk_f16_f32 v150, v180, v181
	v_cvt_pk_f16_f32 v151, v182, v183
	global_load_dwordx4 v[168:171], v[140:141], off offset:192
	global_load_dwordx4 v[172:175], v[140:141], off offset:208
	global_load_dwordx4 v[176:179], v[138:139], off offset:192
	global_load_dwordx4 v[180:183], v[138:139], off offset:208
	v_cvt_pk_f16_f32 v152, v184, v188
	v_cvt_pk_f16_f32 v153, v192, v196
	v_cvt_pk_f16_f32 v154, v200, v204
	v_cvt_pk_f16_f32 v155, v208, v212
	v_cvt_pk_f16_f32 v156, v185, v189
	v_cvt_pk_f16_f32 v157, v193, v197
	v_cvt_pk_f16_f32 v158, v201, v205
	v_cvt_pk_f16_f32 v159, v209, v213
	v_cvt_pk_f16_f32 v160, v186, v190
	v_cvt_pk_f16_f32 v161, v194, v198
	v_cvt_pk_f16_f32 v162, v202, v206
	v_cvt_pk_f16_f32 v163, v210, v214
	v_cvt_pk_f16_f32 v164, v187, v191
	v_cvt_pk_f16_f32 v165, v195, v199
	v_cvt_pk_f16_f32 v166, v203, v207
	v_cvt_pk_f16_f32 v167, v211, v215
	s_nop 1
	v_mfma_f32_32x32x16_f16 v[98:113], v[144:147], v[152:155], v[98:113]
	v_mfma_f32_32x32x16_f16 v[66:81], v[148:151], v[152:155], v[66:81]
	v_mfma_f32_32x32x16_f16 v[34:49], v[144:147], v[156:159], v[34:49]
	v_mfma_f32_32x32x16_f16 v[2:17], v[148:151], v[156:159], v[2:17]
	v_mfma_f32_32x32x16_f16 v[114:129], v[144:147], v[160:163], v[114:129]
	v_mfma_f32_32x32x16_f16 v[82:97], v[148:151], v[160:163], v[82:97]
	v_mfma_f32_32x32x16_f16 v[50:65], v[144:147], v[164:167], v[50:65]
	v_mfma_f32_32x32x16_f16 v[18:33], v[148:151], v[164:167], v[18:33]
	s_add_u32 s22, s20, 0x400000
	s_addc_u32 s23, s21, 0
	global_load_dwordx4 v[184:187], v248, s[22:23]
	s_add_u32 s22, s20, 0x410000
	s_addc_u32 s23, s21, 0
	global_load_dwordx4 v[188:191], v248, s[22:23]
	s_add_u32 s22, s20, 0x420000
	s_addc_u32 s23, s21, 0
	global_load_dwordx4 v[192:195], v248, s[22:23]
	s_add_u32 s22, s20, 0x430000
	s_addc_u32 s23, s21, 0
	global_load_dwordx4 v[196:199], v248, s[22:23]
	s_add_u32 s22, s20, 0x440000
	s_addc_u32 s23, s21, 0
	global_load_dwordx4 v[200:203], v248, s[22:23]
	s_add_u32 s22, s20, 0x450000
	s_addc_u32 s23, s21, 0
	global_load_dwordx4 v[204:207], v248, s[22:23]
	s_add_u32 s22, s20, 0x460000
	s_addc_u32 s23, s21, 0
	global_load_dwordx4 v[208:211], v248, s[22:23]
	s_add_u32 s22, s20, 0x470000
	s_addc_u32 s23, s21, 0
	global_load_dwordx4 v[212:215], v248, s[22:23]
	s_waitcnt vmcnt(8)
	v_pk_mul_f32 v[168:169], v[168:169], v[132:133] op_sel_hi:[1,0]
	v_pk_mul_f32 v[170:171], v[170:171], v[132:133] op_sel_hi:[1,0]
	v_pk_mul_f32 v[172:173], v[172:173], v[132:133] op_sel_hi:[1,0]
	v_pk_mul_f32 v[174:175], v[174:175], v[132:133] op_sel_hi:[1,0]
	v_pk_mul_f32 v[176:177], v[176:177], v[134:135] op_sel_hi:[1,0]
	v_pk_mul_f32 v[178:179], v[178:179], v[134:135] op_sel_hi:[1,0]
	v_pk_mul_f32 v[180:181], v[180:181], v[134:135] op_sel_hi:[1,0]
	v_pk_mul_f32 v[182:183], v[182:183], v[134:135] op_sel_hi:[1,0]
	v_cvt_pk_f16_f32 v144, v168, v169
	v_cvt_pk_f16_f32 v145, v170, v171
	v_cvt_pk_f16_f32 v146, v172, v173
	v_cvt_pk_f16_f32 v147, v174, v175
	v_cvt_pk_f16_f32 v148, v176, v177
	v_cvt_pk_f16_f32 v149, v178, v179
	v_cvt_pk_f16_f32 v150, v180, v181
	v_cvt_pk_f16_f32 v151, v182, v183
	global_load_dwordx4 v[168:171], v[140:141], off offset:256
	global_load_dwordx4 v[172:175], v[140:141], off offset:272
	global_load_dwordx4 v[176:179], v[138:139], off offset:256
	global_load_dwordx4 v[180:183], v[138:139], off offset:272
	v_cvt_pk_f16_f32 v152, v216, v220
	v_cvt_pk_f16_f32 v153, v224, v228
	v_cvt_pk_f16_f32 v154, v232, v236
	v_cvt_pk_f16_f32 v155, v240, v244
	v_cvt_pk_f16_f32 v156, v217, v221
	v_cvt_pk_f16_f32 v157, v225, v229
	v_cvt_pk_f16_f32 v158, v233, v237
	v_cvt_pk_f16_f32 v159, v241, v245
	v_cvt_pk_f16_f32 v160, v218, v222
	v_cvt_pk_f16_f32 v161, v226, v230
	v_cvt_pk_f16_f32 v162, v234, v238
	v_cvt_pk_f16_f32 v163, v242, v246
	v_cvt_pk_f16_f32 v164, v219, v223
	v_cvt_pk_f16_f32 v165, v227, v231
	v_cvt_pk_f16_f32 v166, v235, v239
	v_cvt_pk_f16_f32 v167, v243, v247
	s_nop 1
	v_mfma_f32_32x32x16_f16 v[98:113], v[144:147], v[152:155], v[98:113]
	v_mfma_f32_32x32x16_f16 v[66:81], v[148:151], v[152:155], v[66:81]
	v_mfma_f32_32x32x16_f16 v[34:49], v[144:147], v[156:159], v[34:49]
	v_mfma_f32_32x32x16_f16 v[2:17], v[148:151], v[156:159], v[2:17]
	v_mfma_f32_32x32x16_f16 v[114:129], v[144:147], v[160:163], v[114:129]
	v_mfma_f32_32x32x16_f16 v[82:97], v[148:151], v[160:163], v[82:97]
	v_mfma_f32_32x32x16_f16 v[50:65], v[144:147], v[164:167], v[50:65]
	v_mfma_f32_32x32x16_f16 v[18:33], v[148:151], v[164:167], v[18:33]
	s_add_u32 s22, s20, 0x500000
	s_addc_u32 s23, s21, 0
	global_load_dwordx4 v[216:219], v248, s[22:23]
	s_add_u32 s22, s20, 0x510000
	s_addc_u32 s23, s21, 0
	global_load_dwordx4 v[220:223], v248, s[22:23]
	s_add_u32 s22, s20, 0x520000
	s_addc_u32 s23, s21, 0
	global_load_dwordx4 v[224:227], v248, s[22:23]
	s_add_u32 s22, s20, 0x530000
	s_addc_u32 s23, s21, 0
	global_load_dwordx4 v[228:231], v248, s[22:23]
	s_add_u32 s22, s20, 0x540000
	s_addc_u32 s23, s21, 0
	global_load_dwordx4 v[232:235], v248, s[22:23]
	s_add_u32 s22, s20, 0x550000
	s_addc_u32 s23, s21, 0
	global_load_dwordx4 v[236:239], v248, s[22:23]
	s_add_u32 s22, s20, 0x560000
	s_addc_u32 s23, s21, 0
	global_load_dwordx4 v[240:243], v248, s[22:23]
	s_add_u32 s22, s20, 0x570000
	s_addc_u32 s23, s21, 0
	global_load_dwordx4 v[244:247], v248, s[22:23]
	s_waitcnt vmcnt(8)
	v_pk_mul_f32 v[168:169], v[168:169], v[132:133] op_sel_hi:[1,0]
	v_pk_mul_f32 v[170:171], v[170:171], v[132:133] op_sel_hi:[1,0]
	v_pk_mul_f32 v[172:173], v[172:173], v[132:133] op_sel_hi:[1,0]
	v_pk_mul_f32 v[174:175], v[174:175], v[132:133] op_sel_hi:[1,0]
	v_pk_mul_f32 v[176:177], v[176:177], v[134:135] op_sel_hi:[1,0]
	v_pk_mul_f32 v[178:179], v[178:179], v[134:135] op_sel_hi:[1,0]
	v_pk_mul_f32 v[180:181], v[180:181], v[134:135] op_sel_hi:[1,0]
	v_pk_mul_f32 v[182:183], v[182:183], v[134:135] op_sel_hi:[1,0]
	v_cvt_pk_f16_f32 v144, v168, v169
	v_cvt_pk_f16_f32 v145, v170, v171
	v_cvt_pk_f16_f32 v146, v172, v173
	v_cvt_pk_f16_f32 v147, v174, v175
	v_cvt_pk_f16_f32 v148, v176, v177
	v_cvt_pk_f16_f32 v149, v178, v179
	v_cvt_pk_f16_f32 v150, v180, v181
	v_cvt_pk_f16_f32 v151, v182, v183
	global_load_dwordx4 v[168:171], v[140:141], off offset:320
	global_load_dwordx4 v[172:175], v[140:141], off offset:336
	global_load_dwordx4 v[176:179], v[138:139], off offset:320
	global_load_dwordx4 v[180:183], v[138:139], off offset:336
	v_cvt_pk_f16_f32 v152, v184, v188
	v_cvt_pk_f16_f32 v153, v192, v196
	v_cvt_pk_f16_f32 v154, v200, v204
	v_cvt_pk_f16_f32 v155, v208, v212
	v_cvt_pk_f16_f32 v156, v185, v189
	v_cvt_pk_f16_f32 v157, v193, v197
	v_cvt_pk_f16_f32 v158, v201, v205
	v_cvt_pk_f16_f32 v159, v209, v213
	v_cvt_pk_f16_f32 v160, v186, v190
	v_cvt_pk_f16_f32 v161, v194, v198
	v_cvt_pk_f16_f32 v162, v202, v206
	v_cvt_pk_f16_f32 v163, v210, v214
	v_cvt_pk_f16_f32 v164, v187, v191
	v_cvt_pk_f16_f32 v165, v195, v199
	v_cvt_pk_f16_f32 v166, v203, v207
	v_cvt_pk_f16_f32 v167, v211, v215
	s_nop 1
	v_mfma_f32_32x32x16_f16 v[98:113], v[144:147], v[152:155], v[98:113]
	v_mfma_f32_32x32x16_f16 v[66:81], v[148:151], v[152:155], v[66:81]
	v_mfma_f32_32x32x16_f16 v[34:49], v[144:147], v[156:159], v[34:49]
	v_mfma_f32_32x32x16_f16 v[2:17], v[148:151], v[156:159], v[2:17]
	v_mfma_f32_32x32x16_f16 v[114:129], v[144:147], v[160:163], v[114:129]
	v_mfma_f32_32x32x16_f16 v[82:97], v[148:151], v[160:163], v[82:97]
	v_mfma_f32_32x32x16_f16 v[50:65], v[144:147], v[164:167], v[50:65]
	v_mfma_f32_32x32x16_f16 v[18:33], v[148:151], v[164:167], v[18:33]
	s_waitcnt vmcnt(0)
	v_pk_mul_f32 v[168:169], v[168:169], v[132:133] op_sel_hi:[1,0]
	v_pk_mul_f32 v[170:171], v[170:171], v[132:133] op_sel_hi:[1,0]
	v_pk_mul_f32 v[172:173], v[172:173], v[132:133] op_sel_hi:[1,0]
	v_pk_mul_f32 v[174:175], v[174:175], v[132:133] op_sel_hi:[1,0]
	v_pk_mul_f32 v[176:177], v[176:177], v[134:135] op_sel_hi:[1,0]
	v_pk_mul_f32 v[178:179], v[178:179], v[134:135] op_sel_hi:[1,0]
	v_pk_mul_f32 v[180:181], v[180:181], v[134:135] op_sel_hi:[1,0]
	v_pk_mul_f32 v[182:183], v[182:183], v[134:135] op_sel_hi:[1,0]
	v_cvt_pk_f16_f32 v144, v168, v169
	v_cvt_pk_f16_f32 v145, v170, v171
	v_cvt_pk_f16_f32 v146, v172, v173
	v_cvt_pk_f16_f32 v147, v174, v175
	v_cvt_pk_f16_f32 v148, v176, v177
	v_cvt_pk_f16_f32 v149, v178, v179
	v_cvt_pk_f16_f32 v150, v180, v181
	v_cvt_pk_f16_f32 v151, v182, v183
	v_cvt_pk_f16_f32 v152, v216, v220
	v_cvt_pk_f16_f32 v153, v224, v228
	v_cvt_pk_f16_f32 v154, v232, v236
	v_cvt_pk_f16_f32 v155, v240, v244
	v_cvt_pk_f16_f32 v156, v217, v221
	v_cvt_pk_f16_f32 v157, v225, v229
	v_cvt_pk_f16_f32 v158, v233, v237
	v_cvt_pk_f16_f32 v159, v241, v245
	v_cvt_pk_f16_f32 v160, v218, v222
	v_cvt_pk_f16_f32 v161, v226, v230
	v_cvt_pk_f16_f32 v162, v234, v238
	v_cvt_pk_f16_f32 v163, v242, v246
	v_cvt_pk_f16_f32 v164, v219, v223
	v_cvt_pk_f16_f32 v165, v227, v231
	v_cvt_pk_f16_f32 v166, v235, v239
	v_cvt_pk_f16_f32 v167, v243, v247
	s_nop 1
	v_mfma_f32_32x32x16_f16 v[98:113], v[144:147], v[152:155], v[98:113]
	v_mfma_f32_32x32x16_f16 v[66:81], v[148:151], v[152:155], v[66:81]
	v_mfma_f32_32x32x16_f16 v[34:49], v[144:147], v[156:159], v[34:49]
	v_mfma_f32_32x32x16_f16 v[2:17], v[148:151], v[156:159], v[2:17]
	v_mfma_f32_32x32x16_f16 v[114:129], v[144:147], v[160:163], v[114:129]
	v_mfma_f32_32x32x16_f16 v[82:97], v[148:151], v[160:163], v[82:97]
	v_mfma_f32_32x32x16_f16 v[50:65], v[144:147], v[164:167], v[50:65]
	v_mfma_f32_32x32x16_f16 v[18:33], v[148:151], v[164:167], v[18:33]
	v_cmp_eq_u32_e32 vcc, 0, v135
	v_and_b32_e32 v132, 63, v0
	v_lshlrev_b32_e32 v0, 2, v132
	v_lshl_or_b32 v140, v143, 15, v0
	v_lshlrev_b32_e32 v141, 14, v135
	v_or_b32_e32 v130, v140, v141
	s_nop 15
	s_cbranch_vccz .Lk1_role1
	ds_write2st64_b32 v130, v114, v115 offset1:1
	ds_write2st64_b32 v130, v116, v117 offset0:2 offset1:3
	ds_write2st64_b32 v130, v118, v119 offset0:4 offset1:5
	ds_write2st64_b32 v130, v120, v121 offset0:6 offset1:7
	ds_write2st64_b32 v130, v122, v123 offset0:8 offset1:9
	ds_write2st64_b32 v130, v124, v125 offset0:10 offset1:11
	ds_write2st64_b32 v130, v126, v127 offset0:12 offset1:13
	ds_write2st64_b32 v130, v128, v129 offset0:14 offset1:15
	ds_write2st64_b32 v130, v82, v83 offset0:16 offset1:17
	ds_write2st64_b32 v130, v84, v85 offset0:18 offset1:19
	ds_write2st64_b32 v130, v86, v87 offset0:20 offset1:21
	ds_write2st64_b32 v130, v88, v89 offset0:22 offset1:23
	ds_write2st64_b32 v130, v90, v91 offset0:24 offset1:25
	ds_write2st64_b32 v130, v92, v93 offset0:26 offset1:27
	ds_write2st64_b32 v130, v94, v95 offset0:28 offset1:29
	ds_write2st64_b32 v130, v96, v97 offset0:30 offset1:31
	ds_write2st64_b32 v130, v50, v51 offset0:32 offset1:33
	ds_write2st64_b32 v130, v52, v53 offset0:34 offset1:35
	ds_write2st64_b32 v130, v54, v55 offset0:36 offset1:37
	ds_write2st64_b32 v130, v56, v57 offset0:38 offset1:39
	ds_write2st64_b32 v130, v58, v59 offset0:40 offset1:41
	ds_write2st64_b32 v130, v60, v61 offset0:42 offset1:43
	ds_write2st64_b32 v130, v62, v63 offset0:44 offset1:45
	ds_write2st64_b32 v130, v64, v65 offset0:46 offset1:47
	ds_write2st64_b32 v130, v18, v19 offset0:48 offset1:49
	ds_write2st64_b32 v130, v20, v21 offset0:50 offset1:51
	ds_write2st64_b32 v130, v22, v23 offset0:52 offset1:53
	ds_write2st64_b32 v130, v24, v25 offset0:54 offset1:55
	ds_write2st64_b32 v130, v26, v27 offset0:56 offset1:57
	ds_write2st64_b32 v130, v28, v29 offset0:58 offset1:59
	ds_write2st64_b32 v130, v30, v31 offset0:60 offset1:61
	ds_write2st64_b32 v130, v32, v33 offset0:62 offset1:63
	v_lshlrev_b32_e32 v0, 2, v1
	v_lshl_or_b32 v143, v135, 1, v0
	v_mbcnt_lo_u32_b32 v0, -1, 0
	v_mbcnt_hi_u32_b32 v0, -1, v0
	v_and_b32_e32 v130, 64, v0
	v_xor_b32_e32 v1, 32, v0
	v_add_u32_e32 v130, 64, v130
	v_cmp_lt_i32_e64 s[0:1], v1, v130
	v_lshlrev_b32_e32 v130, 1, v142
	s_waitcnt lgkmcnt(0)
	v_cndmask_b32_e64 v0, v0, v1, s[0:1]
	v_lshlrev_b32_e32 v144, 2, v0
	v_xor_b32_e32 v0, 0x4000, v141
	v_or_b32_e32 v142, v140, v0
	s_barrier
	ds_read2st64_b32 v[0:1], v142 offset1:1
	ds_read2st64_b32 v[134:135], v142 offset0:4 offset1:5
	ds_read2st64_b32 v[136:137], v142 offset0:6 offset1:7
	ds_read2st64_b32 v[138:139], v142 offset0:2 offset1:3
	s_waitcnt lgkmcnt(3)
	v_add_f32_e32 v0, v98, v0
	s_waitcnt lgkmcnt(2)
	v_add_f32_e32 v98, v102, v134
	v_add_f32_e32 v1, v99, v1
	v_add_f32_e32 v99, v103, v135
	s_waitcnt lgkmcnt(0)
	v_add_f32_e32 v100, v100, v138
	v_add_f32_e32 v102, v104, v136
	v_add_f32_e32 v101, v101, v139
	v_cvt_pk_f16_f32 v104, v0, v1
	v_add_f32_e32 v0, v105, v137
	v_cvt_pk_f16_f32 v100, v100, v101
	v_cvt_pk_f16_f32 v101, v98, v99
	v_cvt_pk_f16_f32 v102, v102, v0
	v_cmp_gt_u32_e64 s[0:1], 32, v132
	v_mov_b32_e32 v120, 0x3c00
	v_bfrev_b32_e32 v121, 60
	s_nop 1
	v_permlane32_swap_b32_e32 v100, v102
	v_permlane32_swap_b32_e32 v104, v101
	s_nop 0
	v_lshlrev_b32_e32 v145, 7, v133
	s_waitcnt lgkmcnt(1)
	v_mov_b32_e32 v99, v100
	v_mov_b32_e32 v100, v102
	s_waitcnt lgkmcnt(0)
	v_mov_b32_e32 v102, v101
	v_cndmask_b32_e64 v103, v120, v102, s[0:1]
	v_cndmask_b32_e64 v101, v121, v100, s[0:1]
	v_mov_b32_e32 v98, v104
	v_bfi_b32 v101, s2, v100, v101
	v_bfi_b32 v100, s2, v103, v102
	ds_read2st64_b32 v[102:103], v142 offset0:8 offset1:9
	ds_read2st64_b32 v[104:105], v142 offset0:12 offset1:13
	ds_read2st64_b32 v[114:115], v142 offset0:14 offset1:15
	ds_read2st64_b32 v[116:117], v142 offset0:10 offset1:11
	v_or_b32_e32 v119, v143, v145
	v_lshl_add_u64 v[0:1], s[8:9], 0, v[130:131]
	s_waitcnt lgkmcnt(3)
	v_add_f32_e32 v102, v106, v102
	v_add_f32_e32 v103, v107, v103
	s_waitcnt lgkmcnt(2)
	v_add_f32_e32 v105, v111, v105
	v_add_f32_e32 v104, v110, v104
	s_waitcnt lgkmcnt(0)
	v_add_f32_e32 v106, v108, v116
	v_add_f32_e32 v107, v112, v114
	v_add_f32_e32 v108, v109, v117
	v_cvt_pk_f16_f32 v110, v102, v103
	v_add_f32_e32 v102, v113, v115
	v_cvt_pk_f16_f32 v106, v106, v108
	v_cvt_pk_f16_f32 v104, v104, v105
	v_cvt_pk_f16_f32 v105, v107, v102
	s_nop 1
	v_permlane32_swap_b32_e32 v106, v105
	v_permlane32_swap_b32_e32 v110, v104
	s_nop 0
	v_add_u32_e32 v130, s3, v119
	v_lshlrev_b64 v[102:103], 5, v[130:131]
	v_lshl_add_u64 v[102:103], v[0:1], 0, v[102:103]
	global_store_dwordx4 v[102:103], v[98:101], off
	s_waitcnt lgkmcnt(0)
	v_mov_b32_e32 v102, v104
	v_mov_b32_e32 v100, v105
	v_xor_b32_e32 v82, 0x5000, v141
	v_mov_b32_e32 v98, v110
	v_cndmask_b32_e64 v103, v120, v102, s[0:1]
	v_cndmask_b32_e64 v101, v121, v100, s[0:1]
	v_or_b32_e32 v110, v140, v82
	v_mov_b32_e32 v99, v106
	v_bfi_b32 v101, s2, v100, v101
	v_bfi_b32 v100, s2, v103, v102
	ds_read2st64_b32 v[102:103], v110 offset1:1
	ds_read2st64_b32 v[104:105], v110 offset0:4 offset1:5
	ds_read2st64_b32 v[106:107], v110 offset0:6 offset1:7
	ds_read2st64_b32 v[108:109], v110 offset0:2 offset1:3
	s_waitcnt lgkmcnt(3)
	v_add_f32_e32 v66, v66, v102
	v_add_f32_e32 v67, v67, v103
	s_waitcnt lgkmcnt(2)
	v_add_f32_e32 v70, v70, v104
	v_add_f32_e32 v71, v71, v105
	s_waitcnt lgkmcnt(0)
	v_add_f32_e32 v68, v68, v108
	v_add_f32_e32 v72, v72, v106
	v_add_f32_e32 v69, v69, v109
	v_cvt_pk_f16_f32 v82, v66, v67
	v_add_f32_e32 v66, v73, v107
	v_cvt_pk_f16_f32 v68, v68, v69
	v_cvt_pk_f16_f32 v69, v70, v71
	v_cvt_pk_f16_f32 v70, v72, v66
	s_nop 1
	v_permlane32_swap_b32_e32 v68, v70
	v_permlane32_swap_b32_e32 v82, v69
	s_nop 0
	v_lshl_add_u32 v118, v143, 7, v133
	v_add_u32_e32 v130, s4, v118
	v_lshlrev_b64 v[66:67], 5, v[130:131]
	v_lshl_add_u64 v[66:67], v[0:1], 0, v[66:67]
	global_store_dwordx4 v[66:67], v[98:101], off
	s_waitcnt lgkmcnt(1)
	v_mov_b32_e32 v67, v68
	v_mov_b32_e32 v68, v70
	s_waitcnt lgkmcnt(0)
	v_mov_b32_e32 v70, v69
	v_cndmask_b32_e64 v71, v120, v70, s[0:1]
	v_cndmask_b32_e64 v69, v121, v68, s[0:1]
	v_mov_b32_e32 v66, v82
	v_bfi_b32 v69, s2, v68, v69
	v_bfi_b32 v68, s2, v71, v70
	ds_read2st64_b32 v[70:71], v110 offset0:8 offset1:9
	ds_read2st64_b32 v[72:73], v110 offset0:12 offset1:13
	ds_read2st64_b32 v[82:83], v110 offset0:14 offset1:15
	ds_read2st64_b32 v[84:85], v110 offset0:10 offset1:11
	s_waitcnt lgkmcnt(3)
	v_add_f32_e32 v70, v74, v70
	v_add_f32_e32 v71, v75, v71
	s_waitcnt lgkmcnt(2)
	v_add_f32_e32 v73, v79, v73
	v_add_f32_e32 v72, v78, v72
	s_waitcnt lgkmcnt(0)
	v_add_f32_e32 v74, v76, v84
	v_add_f32_e32 v75, v80, v82
	v_add_f32_e32 v76, v77, v85
	v_cvt_pk_f16_f32 v78, v70, v71
	v_add_f32_e32 v70, v81, v83
	v_cvt_pk_f16_f32 v74, v74, v76
	v_cvt_pk_f16_f32 v72, v72, v73
	v_cvt_pk_f16_f32 v73, v75, v70
	s_nop 1
	v_permlane32_swap_b32_e32 v74, v73
	v_permlane32_swap_b32_e32 v78, v72
	s_nop 0
	v_add_u32_e32 v130, s5, v119
	v_lshlrev_b64 v[70:71], 5, v[130:131]
	v_lshl_add_u64 v[70:71], v[0:1], 0, v[70:71]
	global_store_dwordx4 v[70:71], v[66:69], off
	s_waitcnt lgkmcnt(0)
	v_mov_b32_e32 v70, v72
	v_cndmask_b32_e64 v71, v120, v70, s[0:1]
	v_mov_b32_e32 v68, v73
	v_cndmask_b32_e64 v69, v121, v68, s[0:1]
	v_add_u32_e32 v130, s6, v118
	v_bfi_b32 v69, s2, v68, v69
	v_bfi_b32 v68, s2, v71, v70
	v_lshlrev_b64 v[70:71], 5, v[130:131]
	v_mov_b32_e32 v67, v74
	v_mov_b32_e32 v66, v78
	v_lshl_add_u64 v[70:71], v[0:1], 0, v[70:71]
	v_xor_b32_e32 v50, 0x6000, v141
	global_store_dwordx4 v[70:71], v[66:69], off
	v_or_b32_e32 v74, v140, v50
	ds_read2st64_b32 v[66:67], v74 offset1:1
	ds_read2st64_b32 v[68:69], v74 offset0:4 offset1:5
	ds_read2st64_b32 v[70:71], v74 offset0:6 offset1:7
	ds_read2st64_b32 v[72:73], v74 offset0:2 offset1:3
	s_waitcnt lgkmcnt(3)
	v_add_f32_e32 v34, v34, v66
	v_add_f32_e32 v35, v35, v67
	s_waitcnt lgkmcnt(0)
	v_add_f32_e32 v36, v36, v72
	v_add_f32_e32 v37, v37, v73
	v_add_f32_e32 v38, v38, v68
	v_add_f32_e32 v39, v39, v69
	v_add_f32_e32 v40, v40, v70
	v_cvt_pk_f16_f32 v34, v34, v35
	v_cvt_pk_f16_f32 v35, v36, v37
	v_add_f32_e32 v36, v41, v71
	v_cvt_pk_f16_f32 v37, v38, v39
	v_cvt_pk_f16_f32 v36, v40, v36
	s_nop 1
	v_permlane32_swap_b32_e32 v35, v36
	v_permlane32_swap_b32_e32 v34, v37
	s_nop 0
	v_or_b32_e32 v40, 1, v143
	v_lshl_add_u32 v54, v40, 7, v133
	v_or_b32_e32 v55, v40, v145
	s_waitcnt lgkmcnt(1)
	s_nop 0
	s_nop 0
	s_waitcnt lgkmcnt(0)
	v_mov_b32_e32 v38, v37
	s_nop 0
	v_cndmask_b32_e64 v39, v120, v38, s[0:1]
	v_cndmask_b32_e64 v37, v121, v36, s[0:1]
	v_bfi_b32 v37, s2, v36, v37
	v_bfi_b32 v36, s2, v39, v38
	ds_read2st64_b32 v[38:39], v74 offset0:8 offset1:9
	ds_read2st64_b32 v[40:41], v74 offset0:12 offset1:13
	ds_read2st64_b32 v[50:51], v74 offset0:14 offset1:15
	ds_read2st64_b32 v[52:53], v74 offset0:10 offset1:11
	s_waitcnt lgkmcnt(3)
	v_add_f32_e32 v38, v42, v38
	v_add_f32_e32 v39, v43, v39
	s_waitcnt lgkmcnt(2)
	v_add_f32_e32 v41, v47, v41
	v_add_f32_e32 v40, v46, v40
	s_waitcnt lgkmcnt(0)
	v_add_f32_e32 v42, v44, v52
	v_add_f32_e32 v43, v48, v50
	v_add_f32_e32 v44, v45, v53
	v_cvt_pk_f16_f32 v46, v38, v39
	v_add_f32_e32 v38, v49, v51
	v_cvt_pk_f16_f32 v42, v42, v44
	v_cvt_pk_f16_f32 v40, v40, v41
	v_cvt_pk_f16_f32 v41, v43, v38
	s_nop 1
	v_permlane32_swap_b32_e32 v42, v41
	v_permlane32_swap_b32_e32 v46, v40
	s_nop 0
	v_add_u32_e32 v130, s3, v55
	v_lshlrev_b64 v[38:39], 5, v[130:131]
	v_lshl_add_u64 v[38:39], v[0:1], 0, v[38:39]
	global_store_dwordx4 v[38:39], v[34:37], off
	s_waitcnt lgkmcnt(0)
	v_mov_b32_e32 v38, v40
	v_mov_b32_e32 v36, v41
	v_xor_b32_e32 v18, 0x7000, v141
	v_cndmask_b32_e64 v39, v120, v38, s[0:1]
	v_cndmask_b32_e64 v37, v121, v36, s[0:1]
	v_or_b32_e32 v18, v140, v18
	v_mov_b32_e32 v35, v42
	v_mov_b32_e32 v34, v46
	v_bfi_b32 v37, s2, v36, v37
	v_bfi_b32 v36, s2, v39, v38
	ds_read2st64_b32 v[38:39], v18 offset1:1
	ds_read2st64_b32 v[40:41], v18 offset0:4 offset1:5
	ds_read2st64_b32 v[42:43], v18 offset0:6 offset1:7
	ds_read2st64_b32 v[44:45], v18 offset0:2 offset1:3
	s_waitcnt lgkmcnt(3)
	v_add_f32_e32 v2, v2, v38
	v_add_f32_e32 v3, v3, v39
	s_waitcnt lgkmcnt(2)
	v_add_f32_e32 v6, v6, v40
	v_add_f32_e32 v7, v7, v41
	s_waitcnt lgkmcnt(0)
	v_add_f32_e32 v4, v4, v44
	v_add_f32_e32 v8, v8, v42
	v_add_f32_e32 v5, v5, v45
	v_cvt_pk_f16_f32 v19, v2, v3
	v_add_f32_e32 v2, v9, v43
	v_cvt_pk_f16_f32 v4, v4, v5
	v_cvt_pk_f16_f32 v5, v6, v7
	v_cvt_pk_f16_f32 v6, v8, v2
	s_nop 1
	v_permlane32_swap_b32_e32 v4, v6
	v_permlane32_swap_b32_e32 v19, v5
	s_nop 0
	v_add_u32_e32 v130, s4, v54
	v_lshlrev_b64 v[2:3], 5, v[130:131]
	v_lshl_add_u64 v[2:3], v[0:1], 0, v[2:3]
	global_store_dwordx4 v[2:3], v[34:37], off
	s_waitcnt lgkmcnt(1)
	v_mov_b32_e32 v3, v4
	v_mov_b32_e32 v4, v6
	s_waitcnt lgkmcnt(0)
	v_mov_b32_e32 v6, v5
	v_cndmask_b32_e64 v7, v120, v6, s[0:1]
	v_cndmask_b32_e64 v5, v121, v4, s[0:1]
	v_mov_b32_e32 v2, v19
	v_bfi_b32 v5, s2, v4, v5
	v_bfi_b32 v4, s2, v7, v6
	ds_read2st64_b32 v[6:7], v18 offset0:8 offset1:9
	ds_read2st64_b32 v[8:9], v18 offset0:12 offset1:13
	v_mov_b32_e32 v19, v10
	v_mov_b32_e32 v21, v11
	ds_read2st64_b32 v[10:11], v18 offset0:14 offset1:15
	v_mov_b32_e32 v20, v14
	v_mov_b32_e32 v22, v15
	ds_read2st64_b32 v[14:15], v18 offset0:10 offset1:11
	s_waitcnt lgkmcnt(3)
	v_add_f32_e32 v6, v19, v6
	v_add_f32_e32 v7, v21, v7
	s_waitcnt lgkmcnt(2)
	v_add_f32_e32 v8, v20, v8
	v_add_f32_e32 v9, v22, v9
	s_waitcnt lgkmcnt(1)
	v_add_f32_e32 v10, v16, v10
	s_waitcnt lgkmcnt(0)
	v_add_f32_e32 v12, v12, v14
	v_add_f32_e32 v13, v13, v15
	v_cvt_pk_f16_f32 v14, v6, v7
	v_add_f32_e32 v6, v17, v11
	v_cvt_pk_f16_f32 v12, v12, v13
	v_cvt_pk_f16_f32 v8, v8, v9
	v_cvt_pk_f16_f32 v9, v10, v6
	s_nop 1
	v_permlane32_swap_b32_e32 v12, v9
	v_permlane32_swap_b32_e32 v14, v8
	s_nop 0
	v_add_u32_e32 v130, s5, v55
	v_lshlrev_b64 v[6:7], 5, v[130:131]
	v_lshl_add_u64 v[6:7], v[0:1], 0, v[6:7]
	global_store_dwordx4 v[6:7], v[2:5], off
	s_waitcnt lgkmcnt(0)
	v_mov_b32_e32 v6, v8
	v_cndmask_b32_e64 v7, v120, v6, s[0:1]
	v_mov_b32_e32 v4, v9
	v_cndmask_b32_e64 v5, v121, v4, s[0:1]
	v_add_u32_e32 v130, s6, v54
	v_bfi_b32 v5, s2, v4, v5
	v_bfi_b32 v4, s2, v7, v6
	v_lshlrev_b64 v[6:7], 5, v[130:131]
	v_mov_b32_e32 v3, v12
	v_mov_b32_e32 v2, v14
	v_lshl_add_u64 v[0:1], v[0:1], 0, v[6:7]
	global_store_dwordx4 v[0:1], v[2:5], off
	s_endpgm
.Lk1_role1:
	ds_write2st64_b32 v130, v98, v99 offset1:1
	ds_write2st64_b32 v130, v100, v101 offset0:2 offset1:3
	ds_write2st64_b32 v130, v102, v103 offset0:4 offset1:5
	ds_write2st64_b32 v130, v104, v105 offset0:6 offset1:7
	ds_write2st64_b32 v130, v106, v107 offset0:8 offset1:9
	ds_write2st64_b32 v130, v108, v109 offset0:10 offset1:11
	ds_write2st64_b32 v130, v110, v111 offset0:12 offset1:13
	ds_write2st64_b32 v130, v112, v113 offset0:14 offset1:15
	ds_write2st64_b32 v130, v66, v67 offset0:16 offset1:17
	ds_write2st64_b32 v130, v68, v69 offset0:18 offset1:19
	ds_write2st64_b32 v130, v70, v71 offset0:20 offset1:21
	ds_write2st64_b32 v130, v72, v73 offset0:22 offset1:23
	ds_write2st64_b32 v130, v74, v75 offset0:24 offset1:25
	ds_write2st64_b32 v130, v76, v77 offset0:26 offset1:27
	ds_write2st64_b32 v130, v78, v79 offset0:28 offset1:29
	ds_write2st64_b32 v130, v80, v81 offset0:30 offset1:31
	ds_write2st64_b32 v130, v34, v35 offset0:32 offset1:33
	ds_write2st64_b32 v130, v36, v37 offset0:34 offset1:35
	ds_write2st64_b32 v130, v38, v39 offset0:36 offset1:37
	ds_write2st64_b32 v130, v40, v41 offset0:38 offset1:39
	ds_write2st64_b32 v130, v42, v43 offset0:40 offset1:41
	ds_write2st64_b32 v130, v44, v45 offset0:42 offset1:43
	ds_write2st64_b32 v130, v46, v47 offset0:44 offset1:45
	ds_write2st64_b32 v130, v48, v49 offset0:46 offset1:47
	ds_write2st64_b32 v130, v2, v3 offset0:48 offset1:49
	ds_write2st64_b32 v130, v4, v5 offset0:50 offset1:51
	ds_write2st64_b32 v130, v6, v7 offset0:52 offset1:53
	ds_write2st64_b32 v130, v8, v9 offset0:54 offset1:55
	ds_write2st64_b32 v130, v10, v11 offset0:56 offset1:57
	ds_write2st64_b32 v130, v12, v13 offset0:58 offset1:59
	ds_write2st64_b32 v130, v14, v15 offset0:60 offset1:61
	ds_write2st64_b32 v130, v16, v17 offset0:62 offset1:63
	v_lshlrev_b32_e32 v0, 2, v1
	v_lshl_or_b32 v143, v135, 1, v0
	v_mbcnt_lo_u32_b32 v0, -1, 0
	v_mbcnt_hi_u32_b32 v0, -1, v0
	v_and_b32_e32 v130, 64, v0
	v_xor_b32_e32 v1, 32, v0
	v_add_u32_e32 v130, 64, v130
	v_cmp_lt_i32_e64 s[0:1], v1, v130
	v_lshlrev_b32_e32 v130, 1, v142
	s_waitcnt lgkmcnt(0)
	v_cndmask_b32_e64 v0, v0, v1, s[0:1]
	v_lshlrev_b32_e32 v144, 2, v0
	v_xor_b32_e32 v0, 0x4000, v141
	v_or_b32_e32 v142, v140, v0
	s_barrier
	ds_read2st64_b32 v[0:1], v142 offset1:1
	ds_read2st64_b32 v[134:135], v142 offset0:4 offset1:5
	ds_read2st64_b32 v[136:137], v142 offset0:6 offset1:7
	ds_read2st64_b32 v[138:139], v142 offset0:2 offset1:3
	s_waitcnt lgkmcnt(3)
	v_add_f32_e32 v0, v114, v0
	s_waitcnt lgkmcnt(2)
	v_add_f32_e32 v98, v118, v134
	v_add_f32_e32 v1, v115, v1
	v_add_f32_e32 v99, v119, v135
	s_waitcnt lgkmcnt(0)
	v_add_f32_e32 v100, v116, v138
	v_add_f32_e32 v102, v120, v136
	v_add_f32_e32 v101, v117, v139
	v_cvt_pk_f16_f32 v104, v0, v1
	v_add_f32_e32 v0, v121, v137
	v_cvt_pk_f16_f32 v100, v100, v101
	v_cvt_pk_f16_f32 v101, v98, v99
	v_cvt_pk_f16_f32 v102, v102, v0
	v_cmp_gt_u32_e64 s[0:1], 32, v132
	v_mov_b32_e32 v120, 0x3c00
	v_mov_b32_e32 v103, v121
	v_bfrev_b32_e32 v121, 60
	s_nop 1
	v_permlane32_swap_b32_e32 v100, v102
	v_permlane32_swap_b32_e32 v104, v101
	s_nop 0
	v_lshlrev_b32_e32 v145, 7, v133
	s_waitcnt lgkmcnt(1)
	v_mov_b32_e32 v99, v100
	v_mov_b32_e32 v100, v102
	s_waitcnt lgkmcnt(0)
	v_mov_b32_e32 v102, v101
	v_cndmask_b32_e64 v103, v120, v102, s[0:1]
	v_cndmask_b32_e64 v101, v121, v100, s[0:1]
	v_mov_b32_e32 v98, v104
	v_bfi_b32 v101, s2, v100, v101
	v_bfi_b32 v100, s2, v103, v102
	ds_read2st64_b32 v[102:103], v142 offset0:8 offset1:9
	ds_read2st64_b32 v[104:105], v142 offset0:12 offset1:13
	ds_read2st64_b32 v[114:115], v142 offset0:14 offset1:15
	ds_read2st64_b32 v[116:117], v142 offset0:10 offset1:11
	v_or_b32_e32 v119, v143, v145
	v_lshl_add_u64 v[0:1], s[8:9], 0, v[130:131]
	s_waitcnt lgkmcnt(3)
	v_add_f32_e32 v102, v122, v102
	v_add_f32_e32 v103, v123, v103
	s_waitcnt lgkmcnt(2)
	v_add_f32_e32 v105, v127, v105
	v_add_f32_e32 v104, v126, v104
	s_waitcnt lgkmcnt(0)
	v_add_f32_e32 v106, v124, v116
	v_add_f32_e32 v107, v128, v114
	v_add_f32_e32 v108, v125, v117
	v_cvt_pk_f16_f32 v110, v102, v103
	v_add_f32_e32 v102, v129, v115
	v_cvt_pk_f16_f32 v106, v106, v108
	v_cvt_pk_f16_f32 v104, v104, v105
	v_cvt_pk_f16_f32 v105, v107, v102
	s_nop 1
	v_permlane32_swap_b32_e32 v106, v105
	v_permlane32_swap_b32_e32 v110, v104
	s_nop 0
	v_add_u32_e32 v130, s3, v119
	v_lshlrev_b64 v[102:103], 5, v[130:131]
	v_lshl_add_u64 v[102:103], v[0:1], 0, v[102:103]
	global_store_dwordx4 v[102:103], v[98:101], off
	s_waitcnt lgkmcnt(0)
	v_mov_b32_e32 v102, v104
	v_mov_b32_e32 v100, v105
	v_mov_b32_e32 v66, v82
	v_xor_b32_e32 v82, 0x5000, v141
	v_mov_b32_e32 v98, v110
	v_cndmask_b32_e64 v103, v120, v102, s[0:1]
	v_cndmask_b32_e64 v101, v121, v100, s[0:1]
	v_or_b32_e32 v110, v140, v82
	v_mov_b32_e32 v99, v106
	v_bfi_b32 v101, s2, v100, v101
	v_bfi_b32 v100, s2, v103, v102
	ds_read2st64_b32 v[102:103], v110 offset1:1
	ds_read2st64_b32 v[104:105], v110 offset0:4 offset1:5
	ds_read2st64_b32 v[106:107], v110 offset0:6 offset1:7
	ds_read2st64_b32 v[108:109], v110 offset0:2 offset1:3
	s_waitcnt lgkmcnt(3)
	v_add_f32_e32 v66, v66, v102
	v_add_f32_e32 v67, v83, v103
	s_waitcnt lgkmcnt(2)
	v_add_f32_e32 v70, v86, v104
	v_add_f32_e32 v71, v87, v105
	s_waitcnt lgkmcnt(0)
	v_add_f32_e32 v68, v84, v108
	v_add_f32_e32 v72, v88, v106
	v_add_f32_e32 v69, v85, v109
	v_cvt_pk_f16_f32 v82, v66, v67
	v_add_f32_e32 v66, v89, v107
	v_cvt_pk_f16_f32 v68, v68, v69
	v_cvt_pk_f16_f32 v69, v70, v71
	v_cvt_pk_f16_f32 v70, v72, v66
	s_nop 1
	v_permlane32_swap_b32_e32 v68, v70
	v_permlane32_swap_b32_e32 v82, v69
	s_nop 0
	v_lshl_add_u32 v118, v143, 7, v133
	v_add_u32_e32 v130, s4, v118
	v_lshlrev_b64 v[66:67], 5, v[130:131]
	v_lshl_add_u64 v[66:67], v[0:1], 0, v[66:67]
	global_store_dwordx4 v[66:67], v[98:101], off
	s_waitcnt lgkmcnt(1)
	v_mov_b32_e32 v67, v68
	v_mov_b32_e32 v68, v70
	s_waitcnt lgkmcnt(0)
	v_mov_b32_e32 v70, v69
	v_cndmask_b32_e64 v71, v120, v70, s[0:1]
	v_cndmask_b32_e64 v69, v121, v68, s[0:1]
	v_mov_b32_e32 v66, v82
	v_bfi_b32 v69, s2, v68, v69
	v_bfi_b32 v68, s2, v71, v70
	ds_read2st64_b32 v[70:71], v110 offset0:8 offset1:9
	ds_read2st64_b32 v[72:73], v110 offset0:12 offset1:13
	ds_read2st64_b32 v[82:83], v110 offset0:14 offset1:15
	ds_read2st64_b32 v[84:85], v110 offset0:10 offset1:11
	s_waitcnt lgkmcnt(3)
	v_add_f32_e32 v70, v90, v70
	v_add_f32_e32 v71, v91, v71
	s_waitcnt lgkmcnt(2)
	v_add_f32_e32 v73, v95, v73
	v_add_f32_e32 v72, v94, v72
	s_waitcnt lgkmcnt(0)
	v_add_f32_e32 v74, v92, v84
	v_add_f32_e32 v75, v96, v82
	v_add_f32_e32 v76, v93, v85
	v_cvt_pk_f16_f32 v78, v70, v71
	v_add_f32_e32 v70, v97, v83
	v_cvt_pk_f16_f32 v74, v74, v76
	v_cvt_pk_f16_f32 v72, v72, v73
	v_cvt_pk_f16_f32 v73, v75, v70
	s_nop 1
	v_permlane32_swap_b32_e32 v74, v73
	v_permlane32_swap_b32_e32 v78, v72
	s_nop 0
	v_add_u32_e32 v130, s5, v119
	v_lshlrev_b64 v[70:71], 5, v[130:131]
	v_lshl_add_u64 v[70:71], v[0:1], 0, v[70:71]
	global_store_dwordx4 v[70:71], v[66:69], off
	s_waitcnt lgkmcnt(0)
	v_mov_b32_e32 v70, v72
	v_cndmask_b32_e64 v71, v120, v70, s[0:1]
	v_mov_b32_e32 v68, v73
	v_cndmask_b32_e64 v69, v121, v68, s[0:1]
	v_add_u32_e32 v130, s6, v118
	v_bfi_b32 v69, s2, v68, v69
	v_bfi_b32 v68, s2, v71, v70
	v_lshlrev_b64 v[70:71], 5, v[130:131]
	v_mov_b32_e32 v67, v74
	v_mov_b32_e32 v66, v78
	v_lshl_add_u64 v[70:71], v[0:1], 0, v[70:71]
	v_mov_b32_e32 v34, v50
	v_xor_b32_e32 v50, 0x6000, v141
	global_store_dwordx4 v[70:71], v[66:69], off
	v_or_b32_e32 v74, v140, v50
	ds_read2st64_b32 v[66:67], v74 offset1:1
	ds_read2st64_b32 v[68:69], v74 offset0:4 offset1:5
	ds_read2st64_b32 v[70:71], v74 offset0:6 offset1:7
	ds_read2st64_b32 v[72:73], v74 offset0:2 offset1:3
	s_waitcnt lgkmcnt(3)
	v_add_f32_e32 v34, v34, v66
	v_add_f32_e32 v35, v51, v67
	s_waitcnt lgkmcnt(0)
	v_add_f32_e32 v36, v52, v72
	v_add_f32_e32 v37, v53, v73
	v_add_f32_e32 v38, v54, v68
	v_add_f32_e32 v39, v55, v69
	v_add_f32_e32 v40, v56, v70
	v_cvt_pk_f16_f32 v34, v34, v35
	v_cvt_pk_f16_f32 v35, v36, v37
	v_add_f32_e32 v36, v57, v71
	v_cvt_pk_f16_f32 v37, v38, v39
	v_cvt_pk_f16_f32 v36, v40, v36
	s_nop 1
	v_permlane32_swap_b32_e32 v35, v36
	v_permlane32_swap_b32_e32 v34, v37
	s_nop 0
	v_or_b32_e32 v40, 1, v143
	v_lshl_add_u32 v54, v40, 7, v133
	v_or_b32_e32 v55, v40, v145
	s_waitcnt lgkmcnt(1)
	s_nop 0
	s_nop 0
	s_waitcnt lgkmcnt(0)
	v_mov_b32_e32 v38, v37
	s_nop 0
	v_cndmask_b32_e64 v39, v120, v38, s[0:1]
	v_cndmask_b32_e64 v37, v121, v36, s[0:1]
	v_bfi_b32 v37, s2, v36, v37
	v_bfi_b32 v36, s2, v39, v38
	ds_read2st64_b32 v[38:39], v74 offset0:8 offset1:9
	ds_read2st64_b32 v[40:41], v74 offset0:12 offset1:13
	ds_read2st64_b32 v[50:51], v74 offset0:14 offset1:15
	ds_read2st64_b32 v[52:53], v74 offset0:10 offset1:11
	s_waitcnt lgkmcnt(3)
	v_add_f32_e32 v38, v58, v38
	v_add_f32_e32 v39, v59, v39
	s_waitcnt lgkmcnt(2)
	v_add_f32_e32 v41, v63, v41
	v_add_f32_e32 v40, v62, v40
	s_waitcnt lgkmcnt(0)
	v_add_f32_e32 v42, v60, v52
	v_add_f32_e32 v43, v64, v50
	v_add_f32_e32 v44, v61, v53
	v_cvt_pk_f16_f32 v46, v38, v39
	v_add_f32_e32 v38, v65, v51
	v_cvt_pk_f16_f32 v42, v42, v44
	v_cvt_pk_f16_f32 v40, v40, v41
	v_cvt_pk_f16_f32 v41, v43, v38
	s_nop 1
	v_permlane32_swap_b32_e32 v42, v41
	v_permlane32_swap_b32_e32 v46, v40
	s_nop 0
	v_add_u32_e32 v130, s3, v55
	v_lshlrev_b64 v[38:39], 5, v[130:131]
	v_lshl_add_u64 v[38:39], v[0:1], 0, v[38:39]
	global_store_dwordx4 v[38:39], v[34:37], off
	s_waitcnt lgkmcnt(0)
	v_mov_b32_e32 v38, v40
	v_mov_b32_e32 v36, v41
	v_mov_b32_e32 v2, v18
	v_xor_b32_e32 v18, 0x7000, v141
	v_cndmask_b32_e64 v39, v120, v38, s[0:1]
	v_cndmask_b32_e64 v37, v121, v36, s[0:1]
	v_or_b32_e32 v18, v140, v18
	v_mov_b32_e32 v35, v42
	v_mov_b32_e32 v34, v46
	v_bfi_b32 v37, s2, v36, v37
	v_bfi_b32 v36, s2, v39, v38
	ds_read2st64_b32 v[38:39], v18 offset1:1
	ds_read2st64_b32 v[40:41], v18 offset0:4 offset1:5
	ds_read2st64_b32 v[42:43], v18 offset0:6 offset1:7
	ds_read2st64_b32 v[44:45], v18 offset0:2 offset1:3
	s_waitcnt lgkmcnt(3)
	v_add_f32_e32 v2, v2, v38
	v_add_f32_e32 v3, v19, v39
	s_waitcnt lgkmcnt(2)
	v_add_f32_e32 v6, v22, v40
	v_add_f32_e32 v7, v23, v41
	s_waitcnt lgkmcnt(0)
	v_add_f32_e32 v4, v20, v44
	v_add_f32_e32 v8, v24, v42
	v_add_f32_e32 v5, v21, v45
	v_cvt_pk_f16_f32 v19, v2, v3
	v_add_f32_e32 v2, v25, v43
	v_cvt_pk_f16_f32 v4, v4, v5
	v_cvt_pk_f16_f32 v5, v6, v7
	v_cvt_pk_f16_f32 v6, v8, v2
	s_nop 1
	v_permlane32_swap_b32_e32 v4, v6
	v_permlane32_swap_b32_e32 v19, v5
	s_nop 0
	v_add_u32_e32 v130, s4, v54
	v_lshlrev_b64 v[2:3], 5, v[130:131]
	v_lshl_add_u64 v[2:3], v[0:1], 0, v[2:3]
	global_store_dwordx4 v[2:3], v[34:37], off
	s_waitcnt lgkmcnt(1)
	v_mov_b32_e32 v3, v4
	v_mov_b32_e32 v4, v6
	s_waitcnt lgkmcnt(0)
	v_mov_b32_e32 v6, v5
	v_cndmask_b32_e64 v7, v120, v6, s[0:1]
	v_cndmask_b32_e64 v5, v121, v4, s[0:1]
	v_mov_b32_e32 v2, v19
	v_bfi_b32 v5, s2, v4, v5
	v_bfi_b32 v4, s2, v7, v6
	ds_read2st64_b32 v[6:7], v18 offset0:8 offset1:9
	ds_read2st64_b32 v[8:9], v18 offset0:12 offset1:13
	ds_read2st64_b32 v[10:11], v18 offset0:14 offset1:15
	ds_read2st64_b32 v[14:15], v18 offset0:10 offset1:11
	s_waitcnt lgkmcnt(3)
	v_add_f32_e32 v6, v26, v6
	v_add_f32_e32 v7, v27, v7
	s_waitcnt lgkmcnt(2)
	v_add_f32_e32 v8, v30, v8
	v_add_f32_e32 v9, v31, v9
	s_waitcnt lgkmcnt(1)
	v_add_f32_e32 v10, v32, v10
	s_waitcnt lgkmcnt(0)
	v_add_f32_e32 v12, v28, v14
	v_add_f32_e32 v13, v29, v15
	v_cvt_pk_f16_f32 v14, v6, v7
	v_add_f32_e32 v6, v33, v11
	v_cvt_pk_f16_f32 v12, v12, v13
	v_cvt_pk_f16_f32 v8, v8, v9
	v_cvt_pk_f16_f32 v9, v10, v6
	s_nop 1
	v_permlane32_swap_b32_e32 v12, v9
	v_permlane32_swap_b32_e32 v14, v8
	s_nop 0
	v_add_u32_e32 v130, s5, v55
	v_lshlrev_b64 v[6:7], 5, v[130:131]
	v_lshl_add_u64 v[6:7], v[0:1], 0, v[6:7]
	global_store_dwordx4 v[6:7], v[2:5], off
	s_waitcnt lgkmcnt(0)
	v_mov_b32_e32 v6, v8
	v_cndmask_b32_e64 v7, v120, v6, s[0:1]
	v_mov_b32_e32 v4, v9
	v_cndmask_b32_e64 v5, v121, v4, s[0:1]
	v_add_u32_e32 v130, s6, v54
	v_bfi_b32 v5, s2, v4, v5
	v_bfi_b32 v4, s2, v7, v6
	v_lshlrev_b64 v[6:7], 5, v[130:131]
	v_mov_b32_e32 v3, v12
	v_mov_b32_e32 v2, v14
	v_lshl_add_u64 v[0:1], v[0:1], 0, v[6:7]
	global_store_dwordx4 v[0:1], v[2:5], off
	s_endpgm

	.amdhsa_kernel _Z11proj_kernelPKfS0_S0_S0_S0_S0_PDF16_S1_PfS2_
		.amdhsa_group_segment_fixed_size 65536
		.amdhsa_private_segment_fixed_size 0
		.amdhsa_kernarg_size 80
		.amdhsa_user_sgpr_count 2
		.amdhsa_user_sgpr_dispatch_ptr 0
		.amdhsa_user_sgpr_queue_ptr 0
		.amdhsa_user_sgpr_kernarg_segment_ptr 1
		.amdhsa_user_sgpr_dispatch_id 0
		.amdhsa_user_sgpr_kernarg_preload_length 0
		.amdhsa_user_sgpr_kernarg_preload_offset 0
		.amdhsa_user_sgpr_private_segment_size 0
		.amdhsa_uses_dynamic_stack 0
		.amdhsa_enable_private_segment 0
		.amdhsa_system_sgpr_workgroup_id_x 1
		.amdhsa_system_sgpr_workgroup_id_y 0
		.amdhsa_system_sgpr_workgroup_id_z 0
		.amdhsa_system_sgpr_workgroup_info 0
		.amdhsa_system_vgpr_workitem_id 0
		.amdhsa_next_free_vgpr 251
		.amdhsa_next_free_sgpr 96
		.amdhsa_accum_offset 252
		.amdhsa_reserve_vcc 1
		.amdhsa_float_round_mode_32 0
		.amdhsa_float_round_mode_16_64 0
		.amdhsa_float_denorm_mode_32 3
		.amdhsa_float_denorm_mode_16_64 3
		.amdhsa_dx10_clamp 1
		.amdhsa_ieee_mode 1
		.amdhsa_fp16_overflow 0
		.amdhsa_tg_split 0
		.amdhsa_exception_fp_ieee_invalid_op 0
		.amdhsa_exception_fp_denorm_src 0
		.amdhsa_exception_fp_ieee_div_zero 0
		.amdhsa_exception_fp_ieee_overflow 0
		.amdhsa_exception_fp_ieee_underflow 0
		.amdhsa_exception_fp_ieee_inexact 0
		.amdhsa_exception_int_div_zero 0
	.end_amdhsa_kernel

amdhsa.kernels:
  - .agpr_count:     0
    .args:
      - .actual_access:  read_only
        .address_space:  global
        .offset:         0
        .size:           8
        .value_kind:     global_buffer
      - .actual_access:  read_only
        .address_space:  global
        .offset:         8
        .size:           8
        .value_kind:     global_buffer
      - .actual_access:  read_only
        .address_space:  global
        .offset:         16
        .size:           8
        .value_kind:     global_buffer
      - .actual_access:  read_only
        .address_space:  global
        .offset:         24
        .size:           8
        .value_kind:     global_buffer
      - .actual_access:  read_only
        .address_space:  global
        .offset:         32
        .size:           8
        .value_kind:     global_buffer
      - .actual_access:  read_only
        .address_space:  global
        .offset:         40
        .size:           8
        .value_kind:     global_buffer
      - .actual_access:  write_only
        .address_space:  global
        .offset:         48
        .size:           8
        .value_kind:     global_buffer
      - .actual_access:  write_only
        .address_space:  global
        .offset:         56
        .size:           8
        .value_kind:     global_buffer
      - .actual_access:  write_only
        .address_space:  global
        .offset:         64
        .size:           8
        .value_kind:     global_buffer
      - .actual_access:  write_only
        .address_space:  global
        .offset:         72
        .size:           8
        .value_kind:     global_buffer
    .group_segment_fixed_size: 65536
    .kernarg_segment_align: 8
    .kernarg_segment_size: 80
    .language:       OpenCL C
    .language_version:
      - 2
      - 0
    .max_flat_workgroup_size: 256
    .name:           _Z11proj_kernelPKfS0_S0_S0_S0_S0_PDF16_S1_PfS2_
    .private_segment_fixed_size: 0
    .sgpr_count:     22
    .sgpr_spill_count: 0
    .symbol:         _Z11proj_kernelPKfS0_S0_S0_S0_S0_PDF16_S1_PfS2_.kd
    .uniform_work_group_size: 1
    .uses_dynamic_stack: false
    .vgpr_count:     251
    .vgpr_spill_count: 0
    .wavefront_size: 64
  - .agpr_count:     0
    .args:
      - .actual_access:  read_only
        .address_space:  global
        .offset:         0
        .size:           8
        .value_kind:     global_buffer
      - .actual_access:  write_only
        .address_space:  global
        .offset:         8
        .size:           8
        .value_kind:     global_buffer
    .group_segment_fixed_size: 12672
    .kernarg_segment_align: 8
    .kernarg_segment_size: 16
    .language:       OpenCL C
    .language_version:
      - 2
      - 0
    .max_flat_workgroup_size: 1024
    .name:           _Z12carry_kernelPKDv2_DF16_PDF16_
    .private_segment_fixed_size: 0
    .sgpr_count:     16
    .sgpr_spill_count: 0
    .symbol:         _Z12carry_kernelPKDv2_DF16_PDF16_.kd
    .uniform_work_group_size: 1
    .uses_dynamic_stack: false
    .vgpr_count:     92
    .vgpr_spill_count: 0
    .wavefront_size: 64
  - .agpr_count:     0
    .args:
      - .actual_access:  read_only
        .address_space:  global
        .offset:         0
        .size:           8
        .value_kind:     global_buffer
      - .actual_access:  read_only
        .address_space:  global
        .offset:         8
        .size:           8
        .value_kind:     global_buffer
      - .actual_access:  read_only
        .address_space:  global
        .offset:         16
        .size:           8
        .value_kind:     global_buffer
      - .actual_access:  read_only
        .address_space:  global
        .offset:         24
        .size:           8
        .value_kind:     global_buffer
      - .actual_access:  read_only
        .address_space:  global
        .offset:         32
        .size:           8
        .value_kind:     global_buffer
      - .actual_access:  write_only
        .address_space:  global
        .offset:         40
        .size:           8
        .value_kind:     global_buffer
      - .actual_access:  read_only
        .address_space:  global
        .offset:         48
        .size:           8
        .value_kind:     global_buffer
      - .actual_access:  read_only
        .address_space:  global
        .offset:         56
        .size:           8
        .value_kind:     global_buffer
    .group_segment_fixed_size: 33280
    .kernarg_segment_align: 8
    .kernarg_segment_size: 64
    .language:       OpenCL C
    .language_version:
      - 2
      - 0
    .max_flat_workgroup_size: 256
    .name:           _Z11scan_kernelILi1ELi1536ELi4EEvPKfPKDF16_S3_S1_S1_PDv2_DF16_S3_Pf
    .private_segment_fixed_size: 0
    .sgpr_count:     24
    .sgpr_spill_count: 0
    .symbol:         _Z11scan_kernelILi1ELi1536ELi4EEvPKfPKDF16_S3_S1_S1_PDv2_DF16_S3_Pf.kd
    .uniform_work_group_size: 1
    .uses_dynamic_stack: false
    .vgpr_count:     110
    .vgpr_spill_count: 0
    .wavefront_size: 64
  - .agpr_count:     0
    .args:
      - .actual_access:  read_only
        .address_space:  global
        .offset:         0
        .size:           8
        .value_kind:     global_buffer
      - .actual_access:  read_only
        .address_space:  global
        .offset:         8
        .size:           8
        .value_kind:     global_buffer
      - .actual_access:  read_only
        .address_space:  global
        .offset:         16
        .size:           8
        .value_kind:     global_buffer
      - .actual_access:  read_only
        .address_space:  global
        .offset:         24
        .size:           8
        .value_kind:     global_buffer
      - .actual_access:  read_only
        .address_space:  global
        .offset:         32
        .size:           8
        .value_kind:     global_buffer
      - .actual_access:  read_only
        .address_space:  global
        .offset:         40
        .size:           8
        .value_kind:     global_buffer
      - .actual_access:  read_only
        .address_space:  global
        .offset:         48
        .size:           8
        .value_kind:     global_buffer
      - .actual_access:  write_only
        .address_space:  global
        .offset:         56
        .size:           8
        .value_kind:     global_buffer
    .group_segment_fixed_size: 50176
    .kernarg_segment_align: 8
    .kernarg_segment_size: 64
    .language:       OpenCL C
    .language_version:
      - 2
      - 0
    .max_flat_workgroup_size: 256
    .name:           _Z11scan_kernelILi3ELi1536ELi3EEvPKfPKDF16_S3_S1_S1_PDv2_DF16_S3_Pf
    .private_segment_fixed_size: 0
    .sgpr_count:     28
    .sgpr_spill_count: 0
    .symbol:         _Z11scan_kernelILi3ELi1536ELi3EEvPKfPKDF16_S3_S1_S1_PDv2_DF16_S3_Pf.kd
    .uniform_work_group_size: 1
    .uses_dynamic_stack: false
    .vgpr_count:     168
    .vgpr_spill_count: 0
    .wavefront_size: 64
